# speedup vs baseline: 1.0751x; 1.0251x over previous
_Z8moe_gemmILi1024ELi2048ELb1EEvPKDF16_S1_PKfPDF16_PfPKiS7_:
	v_lshl_or_b32 v216, s2, 8, v0
	v_and_b32_e32 v217, 63, v216
	v_lshrrev_b32_e32 v216, 6, v216
	v_lshlrev_b32_e32 v215, 3, v217
	v_lshlrev_b32_e32 v214, 4, v217
	v_lshl_add_u32 v217, v216, 10, v215
	v_lshl_add_u32 v216, v216, 11, v214
	s_mov_b32 s96, 16
	s_mov_b32 s97, 0
	s_mov_b32 s98, 0
	s_and_b32 s90, s2, 7
	s_lshr_b32 s91, s2, 3
	v_readfirstlane_b32 s88, v0
	s_load_dwordx2 s[4:5], s[0:1], 0x28
	v_readfirstlane_b32 s12, v0
	s_waitcnt lgkmcnt(0)
	s_load_dwordx2 s[92:93], s[4:5], 0x400
	s_add_u32 s94, s4, 0x6000000
	s_addc_u32 s95, s5, 0
	s_load_dword s23, s[4:5], 0x0
	s_load_dword s25, s[4:5], 0x80
	s_load_dword s27, s[4:5], 0x100
	s_load_dword s29, s[4:5], 0x180
	s_load_dword s31, s[4:5], 0x200
	s_load_dword s33, s[4:5], 0x280
	s_load_dword s35, s[4:5], 0x300
	s_load_dword s38, s[4:5], 0x380
	s_waitcnt lgkmcnt(0)
	s_add_i32 s3, s23, 0x9f
	s_mul_hi_i32 s3, s3, 0x66666667
	s_lshr_b32 s4, s3, 31
	s_ashr_i32 s39, s3, 6
	s_add_i32 s3, s25, 0x9f
	s_mul_hi_i32 s3, s3, 0x66666667
	s_add_i32 s39, s39, s4
	s_lshr_b32 s4, s3, 31
	s_ashr_i32 s40, s3, 6
	s_add_i32 s40, s40, s4
	s_add_i32 s4, s27, 0x9f
	s_mul_hi_i32 s4, s4, 0x66666667
	s_lshr_b32 s5, s4, 31
	s_ashr_i32 s41, s4, 6
	s_add_i32 s4, s29, 0x9f
	s_mul_hi_i32 s4, s4, 0x66666667
	s_add_i32 s41, s41, s5
	s_lshr_b32 s5, s4, 31
	s_ashr_i32 s42, s4, 6
	s_add_i32 s4, s31, 0x9f
	s_mul_hi_i32 s4, s4, 0x66666667
	s_add_i32 s42, s42, s5
	s_lshr_b32 s5, s4, 31
	s_ashr_i32 s43, s4, 6
	s_add_i32 s4, s33, 0x9f
	s_mul_hi_i32 s4, s4, 0x66666667
	s_add_i32 s3, s40, s39
	s_add_i32 s43, s43, s5
	s_lshr_b32 s5, s4, 31
	s_ashr_i32 s44, s4, 6
	s_add_i32 s4, s35, 0x9f
	s_add_i32 s3, s41, s3
	s_mul_hi_i32 s4, s4, 0x66666667
	s_add_i32 s3, s42, s3
	s_add_i32 s44, s44, s5
	s_lshr_b32 s5, s4, 31
	s_ashr_i32 s45, s4, 6
	s_add_i32 s4, s38, 0x9f
	s_add_i32 s3, s43, s3
	s_mul_hi_i32 s4, s4, 0x66666667
	s_add_i32 s3, s44, s3
	s_add_i32 s45, s45, s5
	s_lshr_b32 s5, s4, 31
	s_ashr_i32 s46, s4, 6
	s_add_i32 s3, s45, s3
	s_add_i32 s46, s46, s5
	s_add_i32 s3, s46, s3
	s_lshl_b32 s3, s3, 4
	s_and_b32 s4, s2, 7
	s_mul_i32 s4, s3, s4
	s_lshr_b32 s2, s2, 3
	s_ashr_i32 s5, s4, 3
	s_add_i32 s4, s4, s3
	s_ashr_i32 s47, s4, 3
	s_add_i32 s48, s5, s2
	s_sub_i32 s89, s47, s5
	s_sub_i32 s89, s89, 64
	s_max_i32 s89, s89, 0
	s_min_i32 s89, s89, 64
	s_add_i32 s99, s48, 64
	s_cmp_lt_i32 s99, s47
	s_cselect_b32 s98, 1, 0
	s_cmp_eq_u32 s98, 0
	s_cbranch_scc1 .Las_set
	s_cmp_ge_i32 s89, 64
	s_cbranch_scc1 .Las_set
	s_mov_b32 s96, 8
	s_mov_b32 s98, 3
.Las_set:
	s_cmp_ge_i32 s48, s47
	s_cbranch_scc1 .LBB2_78
	s_load_dword s13, s[0:1], 0x38
	s_load_dwordx2 s[2:3], s[0:1], 0x30
	s_load_dwordx8 s[4:11], s[0:1], 0x0
	v_bfe_u32 v1, v0, 4, 2
	v_lshrrev_b32_e32 v2, 5, v0
	s_waitcnt lgkmcnt(0)
	s_lshr_b32 s49, s13, 3
	s_bfe_u32 s1, s12, 0x10006
	v_and_or_b32 v2, v2, 4, v1
	v_lshrrev_b32_e32 v5, 7, v0
	s_cmpk_lt_u32 s12, 0x80
	v_lshlrev_b32_e32 v2, 4, v2
	v_lshlrev_b32_e32 v3, 3, v0
	s_movk_i32 s0, 0x78
	v_bfe_u32 v4, v0, 4, 3
	v_bitop3_b32 v5, v5, v0, 7 bitop3:0x78
	v_lshlrev_b32_e32 v6, 6, v0
	s_cselect_b64 s[12:13], -1, 0
	v_bitop3_b32 v2, v2, v3, s0 bitop3:0x78
	v_xor_b32_e32 v5, v5, v4
	s_lshl_b32 s0, s1, 6
	v_lshlrev_b32_e32 v4, 2, v1
	v_lshlrev_b32_e32 v1, 11, v1
	v_and_b32_e32 v6, 0x300, v6
	v_and_b32_e32 v8, 8, v3
	v_lshrrev_b32_e32 v101, 4, v0
	v_and_b32_e32 v103, 15, v0
	v_lshrrev_b32_e32 v124, 3, v0
	v_lshl_add_u32 v125, v0, 4, 0
	v_or3_b32 v1, v1, v6, v8
	v_bfe_u32 v6, v0, 1, 3
	v_or_b32_e32 v0, s0, v4
	v_and_b32_e32 v7, 0xe0, v3
	v_lshl_add_u32 v100, v0, 1, 0
	s_lshl_b32 s1, s1, 7
	v_and_b32_e32 v0, 16, v3
	v_or_b32_e32 v3, s1, v0
	v_bitop3_b32 v0, s1, v7, v0 bitop3:0x36
	v_or_b32_e32 v127, v0, v1
	v_bitop3_b32 v0, v3, v7, 32 bitop3:0x36
	v_or_b32_e32 v128, v0, v1
	v_bitop3_b32 v0, v3, v7, 64 bitop3:0x36
	s_movk_i32 s1, 0x60
	v_or_b32_e32 v129, v0, v1
	v_bitop3_b32 v0, v3, v7, s1 bitop3:0x36
	s_add_i32 s1, s23, 15
	s_lshr_b32 s1, s1, 4
	v_or_b32_e32 v130, v0, v1
	s_add_i32 s1, s39, s1
	v_cvt_f32_i32_e32 v0, s39
	s_add_i32 s1, s1, -1
	v_cvt_f32_i32_e32 v1, s1
	s_add_i32 s14, s25, 15
	v_rcp_iflag_f32_e32 v144, v0
	s_lshr_b32 s14, s14, 4
	v_add_f32_e32 v0, 0.5, v1
	v_cvt_f32_i32_e32 v1, s40
	s_add_i32 s14, s40, s14
	s_add_i32 s14, s14, -1
	v_mul_f32_e32 v0, v144, v0
	v_cvt_i32_f32_e32 v0, v0
	v_cvt_f32_i32_e32 v7, s14
	v_rcp_iflag_f32_e32 v145, v1
	s_add_i32 s16, s27, 15
	s_lshr_b32 s16, s16, 4
	v_cvt_f32_i32_e32 v1, s41
	s_add_i32 s16, s41, s16
	v_readfirstlane_b32 s1, v0
	v_add_f32_e32 v0, 0.5, v7
	s_add_i32 s16, s16, -1
	s_add_i32 s17, s29, 15
	s_add_i32 s18, s31, 15
	s_add_i32 s19, s33, 15
	s_add_i32 s20, s35, 15
	s_add_i32 s21, s38, 15
	v_mul_f32_e32 v0, v145, v0
	s_lshr_b32 s17, s17, 4
	s_lshr_b32 s18, s18, 4
	s_lshr_b32 s19, s19, 4
	s_lshr_b32 s20, s20, 4
	s_lshr_b32 s21, s21, 4
	v_cvt_i32_f32_e32 v0, v0
	v_cvt_f32_i32_e32 v7, s16
	s_add_i32 s17, s42, s17
	s_add_i32 s18, s43, s18
	s_add_i32 s19, s44, s19
	s_add_i32 s20, s45, s20
	s_add_i32 s21, s46, s21
	v_rcp_iflag_f32_e32 v146, v1
	s_add_i32 s50, 0, 0xe000
	s_lshl_b32 s52, s39, 4
	s_lshl_b32 s53, s40, 4
	s_lshl_b32 s54, s41, 4
	s_add_i32 s17, s17, -1
	s_lshl_b32 s55, s42, 4
	s_add_i32 s18, s18, -1
	s_lshl_b32 s56, s43, 4
	s_add_i32 s19, s19, -1
	s_lshl_b32 s57, s44, 4
	s_add_i32 s20, s20, -1
	s_lshl_b32 s58, s45, 4
	s_add_i32 s21, s21, -1
	s_lshl_b32 s59, s46, 4
	s_cmp_gt_i32 s23, 0
	v_cvt_f32_i32_e32 v1, s42
	s_cselect_b32 s60, s1, 0
	v_readfirstlane_b32 s1, v0
	v_add_f32_e32 v0, 0.5, v7
	v_mul_f32_e32 v0, v146, v0
	v_cvt_i32_f32_e32 v0, v0
	v_cvt_f32_i32_e32 v7, s17
	v_rcp_iflag_f32_e32 v147, v1
	s_cmp_gt_i32 s25, 0
	v_cvt_f32_i32_e32 v1, s43
	s_cselect_b32 s61, s1, 0
	v_readfirstlane_b32 s1, v0
	v_add_f32_e32 v0, 0.5, v7
	v_mul_f32_e32 v0, v147, v0
	v_cvt_i32_f32_e32 v0, v0
	v_cvt_f32_i32_e32 v7, s18
	v_rcp_iflag_f32_e32 v148, v1
	s_cmp_gt_i32 s27, 0
	v_cvt_f32_i32_e32 v1, s44
	s_cselect_b32 s62, s1, 0
	v_readfirstlane_b32 s1, v0
	v_add_f32_e32 v0, 0.5, v7
	v_mul_f32_e32 v0, v148, v0
	v_cvt_i32_f32_e32 v0, v0
	v_cvt_f32_i32_e32 v7, s19
	v_rcp_iflag_f32_e32 v149, v1
	s_cmp_gt_i32 s29, 0
	v_cvt_f32_i32_e32 v1, s45
	s_cselect_b32 s63, s1, 0
	v_readfirstlane_b32 s1, v0
	v_add_f32_e32 v0, 0.5, v7
	v_mul_f32_e32 v0, v149, v0
	v_cvt_i32_f32_e32 v0, v0
	v_cvt_f32_i32_e32 v7, s20
	v_rcp_iflag_f32_e32 v150, v1
	s_cmp_gt_i32 s31, 0
	s_cselect_b32 s64, s1, 0
	v_readfirstlane_b32 s1, v0
	v_add_f32_e32 v0, 0.5, v7
	v_mul_f32_e32 v0, v150, v0
	v_cvt_i32_f32_e32 v0, v0
	v_cvt_f32_i32_e32 v1, s46
	s_cmp_gt_i32 s33, 0
	s_cselect_b32 s65, s1, 0
	v_readfirstlane_b32 s1, v0
	v_cvt_f32_i32_e32 v0, s21
	v_rcp_iflag_f32_e32 v151, v1
	v_mov_b32_e32 v97, 0
	v_lshlrev_b32_e32 v96, 12, v101
	v_add_f32_e32 v0, 0.5, v0
	v_mul_f32_e32 v0, v151, v0
	v_cvt_i32_f32_e32 v7, v0
	v_lshlrev_b32_e32 v0, 4, v5
	v_mov_b32_e32 v1, v97
	v_lshl_add_u64 v[98:99], s[6:7], 0, v[96:97]
	s_cmp_gt_i32 s35, 0
	v_lshl_add_u64 v[104:105], s[4:5], 0, v[0:1]
	s_mov_b64 s[4:5], 0x80
	v_lshl_or_b32 v96, v2, 1, v96
	v_lshl_add_u32 v8, v103, 4, 0
	v_mul_u32_u24_e32 v3, 0x110, v101
	s_cselect_b32 s66, s1, 0
	s_cmp_gt_i32 s38, 0
	v_readfirstlane_b32 s1, v7
	v_lshl_add_u64 v[106:107], v[104:105], 0, s[4:5]
	v_lshl_add_u64 v[0:1], s[6:7], 0, v[96:97]
	s_mov_b64 s[4:5], 0x40000
	s_mov_b32 s15, 0
	v_lshlrev_b32_e32 v126, 7, v103
	v_lshlrev_b32_e32 v102, 3, v103
	v_add_u32_e32 v131, s50, v127
	v_add_u32_e32 v132, s50, v128
	v_add_u32_e32 v133, s50, v129
	v_add_u32_e32 v134, s50, v130
	s_movk_i32 s51, 0x110
	v_or_b32_e32 v135, 16, v101
	v_or_b32_e32 v136, 32, v101
	v_or_b32_e32 v137, 48, v101
	v_or_b32_e32 v138, 64, v101
	v_or_b32_e32 v139, 0x50, v101
	v_or_b32_e32 v140, 0x60, v101
	v_or_b32_e32 v141, 0x70, v101
	v_or_b32_e32 v142, 0x80, v101
	v_or_b32_e32 v143, 0x90, v101
	v_bitop3_b32 v152, v6, v101, 3 bitop3:0x78
	s_mul_i32 s67, s52, s60
	s_mul_i32 s68, s53, s61
	s_mul_i32 s69, s54, s62
	s_mul_i32 s70, s55, s63
	s_mul_i32 s71, s56, s64
	s_mul_i32 s72, s57, s65
	s_mul_i32 s73, s58, s66
	s_cselect_b32 s74, s1, 0
	v_lshl_add_u64 v[108:109], v[0:1], 0, s[4:5]
	s_lshl_b32 s6, s0, 2
	v_lshlrev_b32_e32 v153, 2, v4
	v_lshlrev_b32_e32 v96, 1, v2
	s_mov_b64 s[16:17], 0x10000
	s_mov_b64 s[18:19], 0x20000
	s_mov_b64 s[20:21], 0x30000
	s_mov_b32 s22, 0x3f3504f3
	s_mov_b32 s75, 0x3ea7ba05
	s_mov_b32 s24, 0xbfba00e3
	s_mov_b32 s26, 0x3f87dc22
	s_mov_b32 s28, 0x3fb5f0e3
	s_brev_b32 s76, -2
	v_add_u32_e32 v154, v8, v3
	s_movk_i32 s77, 0x1080
	s_mov_b32 s30, 0xbe91a98e
	s_mov_b32 s34, 0x3e827906
	s_branch .LBB2_3

.Lw2k_noc:
	s_cmp_eq_u32 s96, 0
	s_cbranch_scc1 .Lw2k_nol
	s_and_b32 s99, s80, s98
	s_cmp_lg_u32 s99, s98
	s_cbranch_scc1 .Lw2k_nol
	global_load_dwordx4 v[208:211], v216, s[92:93] nt
	global_load_dwordx4 v[212:215], v216, s[92:93] offset:1024 nt
	s_add_u32 s92, s92, 0x400000
	s_addc_u32 s93, s93, 0
	s_sub_u32 s96, s96, 1
	s_mov_b32 s97, 1

.Lw2k_end:
	s_cmp_lg_u32 s98, 0
	s_cbranch_scc1 .Las_end
	s_cmp_eq_u32 s89, 0
	s_cbranch_scc1 .Las_end
	s_cmp_ge_i32 s89, 64
	s_cbranch_scc1 .Las_end
	s_sub_i32 s20, s91, s89
	s_sub_i32 s27, 64, s89
	s_lshl_b32 s28, s89, 3
	s_lshr_b32 s29, s88, 6
	s_sub_u32 s64, s92, 0x4000000
	s_subb_u32 s65, s93, 0
	s_sub_u32 s66, s94, 0x2000000
	s_subb_u32 s67, s95, 0
	v_mbcnt_lo_u32_b32 v0, -1, 0
	v_mbcnt_hi_u32_b32 v0, -1, v0
	v_lshlrev_b32_e32 v1, 4, v0
	v_lshlrev_b32_e32 v2, 3, v0
.Las_trip:
	s_cmp_ge_i32 s20, s28
	s_cbranch_scc1 .Las_end
	s_mov_b32 s21, s20
	s_mov_b32 s26, 0
	s_cmp_ge_i32 s21, s28
	s_cbranch_scc1 .Las_issued
	s_lshr_b32 s22, s21, 3
	s_and_b32 s23, s21, 7
	s_lshl_b32 s22, s22, 3
	s_add_i32 s22, s22, s90
	s_lshl_b32 s22, s22, 2
	s_add_i32 s22, s22, s29
	s_add_i32 s23, s23, 8
	s_lshl_b32 s24, s22, 11
	s_lshl_b32 s25, s23, 22
	s_add_u32 s24, s24, s25
	s_add_u32 s30, s64, s24
	s_addc_u32 s31, s65, 0
	s_lshl_b32 s24, s22, 10
	s_lshl_b32 s25, s23, 21
	s_add_u32 s24, s24, s25
	s_add_u32 s32, s66, s24
	s_addc_u32 s33, s67, 0
	global_load_dwordx4 v[8:11], v1, s[30:31] nt
	global_load_dwordx4 v[12:15], v1, s[30:31] offset:1024 nt
	s_add_i32 s21, s21, s27
	s_add_i32 s26, s26, 1
	s_cmp_ge_i32 s21, s28
	s_cbranch_scc1 .Las_issued
	s_lshr_b32 s22, s21, 3
	s_and_b32 s23, s21, 7
	s_lshl_b32 s22, s22, 3
	s_add_i32 s22, s22, s90
	s_lshl_b32 s22, s22, 2
	s_add_i32 s22, s22, s29
	s_add_i32 s23, s23, 8
	s_lshl_b32 s24, s22, 11
	s_lshl_b32 s25, s23, 22
	s_add_u32 s24, s24, s25
	s_add_u32 s34, s64, s24
	s_addc_u32 s35, s65, 0
	s_lshl_b32 s24, s22, 10
	s_lshl_b32 s25, s23, 21
	s_add_u32 s24, s24, s25
	s_add_u32 s36, s66, s24
	s_addc_u32 s37, s67, 0
	global_load_dwordx4 v[16:19], v1, s[34:35] nt
	global_load_dwordx4 v[20:23], v1, s[34:35] offset:1024 nt
	s_add_i32 s21, s21, s27
	s_add_i32 s26, s26, 1
	s_cmp_ge_i32 s21, s28
	s_cbranch_scc1 .Las_issued
	s_lshr_b32 s22, s21, 3
	s_and_b32 s23, s21, 7
	s_lshl_b32 s22, s22, 3
	s_add_i32 s22, s22, s90
	s_lshl_b32 s22, s22, 2
	s_add_i32 s22, s22, s29
	s_add_i32 s23, s23, 8
	s_lshl_b32 s24, s22, 11
	s_lshl_b32 s25, s23, 22
	s_add_u32 s24, s24, s25
	s_add_u32 s38, s64, s24
	s_addc_u32 s39, s65, 0
	s_lshl_b32 s24, s22, 10
	s_lshl_b32 s25, s23, 21
	s_add_u32 s24, s24, s25
	s_add_u32 s40, s66, s24
	s_addc_u32 s41, s67, 0
	global_load_dwordx4 v[24:27], v1, s[38:39] nt
	global_load_dwordx4 v[28:31], v1, s[38:39] offset:1024 nt
	s_add_i32 s21, s21, s27
	s_add_i32 s26, s26, 1
	s_cmp_ge_i32 s21, s28
	s_cbranch_scc1 .Las_issued
	s_lshr_b32 s22, s21, 3
	s_and_b32 s23, s21, 7
	s_lshl_b32 s22, s22, 3
	s_add_i32 s22, s22, s90
	s_lshl_b32 s22, s22, 2
	s_add_i32 s22, s22, s29
	s_add_i32 s23, s23, 8
	s_lshl_b32 s24, s22, 11
	s_lshl_b32 s25, s23, 22
	s_add_u32 s24, s24, s25
	s_add_u32 s42, s64, s24
	s_addc_u32 s43, s65, 0
	s_lshl_b32 s24, s22, 10
	s_lshl_b32 s25, s23, 21
	s_add_u32 s24, s24, s25
	s_add_u32 s44, s66, s24
	s_addc_u32 s45, s67, 0
	global_load_dwordx4 v[32:35], v1, s[42:43] nt
	global_load_dwordx4 v[36:39], v1, s[42:43] offset:1024 nt
	s_add_i32 s21, s21, s27
	s_add_i32 s26, s26, 1
	s_cmp_ge_i32 s21, s28
	s_cbranch_scc1 .Las_issued
	s_lshr_b32 s22, s21, 3
	s_and_b32 s23, s21, 7
	s_lshl_b32 s22, s22, 3
	s_add_i32 s22, s22, s90
	s_lshl_b32 s22, s22, 2
	s_add_i32 s22, s22, s29
	s_add_i32 s23, s23, 8
	s_lshl_b32 s24, s22, 11
	s_lshl_b32 s25, s23, 22
	s_add_u32 s24, s24, s25
	s_add_u32 s46, s64, s24
	s_addc_u32 s47, s65, 0
	s_lshl_b32 s24, s22, 10
	s_lshl_b32 s25, s23, 21
	s_add_u32 s24, s24, s25
	s_add_u32 s48, s66, s24
	s_addc_u32 s49, s67, 0
	global_load_dwordx4 v[40:43], v1, s[46:47] nt
	global_load_dwordx4 v[44:47], v1, s[46:47] offset:1024 nt
	s_add_i32 s21, s21, s27
	s_add_i32 s26, s26, 1
	s_cmp_ge_i32 s21, s28
	s_cbranch_scc1 .Las_issued
	s_lshr_b32 s22, s21, 3
	s_and_b32 s23, s21, 7
	s_lshl_b32 s22, s22, 3
	s_add_i32 s22, s22, s90
	s_lshl_b32 s22, s22, 2
	s_add_i32 s22, s22, s29
	s_add_i32 s23, s23, 8
	s_lshl_b32 s24, s22, 11
	s_lshl_b32 s25, s23, 22
	s_add_u32 s24, s24, s25
	s_add_u32 s50, s64, s24
	s_addc_u32 s51, s65, 0
	s_lshl_b32 s24, s22, 10
	s_lshl_b32 s25, s23, 21
	s_add_u32 s24, s24, s25
	s_add_u32 s52, s66, s24
	s_addc_u32 s53, s67, 0
	global_load_dwordx4 v[48:51], v1, s[50:51] nt
	global_load_dwordx4 v[52:55], v1, s[50:51] offset:1024 nt
	s_add_i32 s21, s21, s27
	s_add_i32 s26, s26, 1
	s_cmp_ge_i32 s21, s28
	s_cbranch_scc1 .Las_issued
	s_lshr_b32 s22, s21, 3
	s_and_b32 s23, s21, 7
	s_lshl_b32 s22, s22, 3
	s_add_i32 s22, s22, s90
	s_lshl_b32 s22, s22, 2
	s_add_i32 s22, s22, s29
	s_add_i32 s23, s23, 8
	s_lshl_b32 s24, s22, 11
	s_lshl_b32 s25, s23, 22
	s_add_u32 s24, s24, s25
	s_add_u32 s54, s64, s24
	s_addc_u32 s55, s65, 0
	s_lshl_b32 s24, s22, 10
	s_lshl_b32 s25, s23, 21
	s_add_u32 s24, s24, s25
	s_add_u32 s56, s66, s24
	s_addc_u32 s57, s67, 0
	global_load_dwordx4 v[56:59], v1, s[54:55] nt
	global_load_dwordx4 v[60:63], v1, s[54:55] offset:1024 nt
	s_add_i32 s21, s21, s27
	s_add_i32 s26, s26, 1
	s_cmp_ge_i32 s21, s28
	s_cbranch_scc1 .Las_issued
	s_lshr_b32 s22, s21, 3
	s_and_b32 s23, s21, 7
	s_lshl_b32 s22, s22, 3
	s_add_i32 s22, s22, s90
	s_lshl_b32 s22, s22, 2
	s_add_i32 s22, s22, s29
	s_add_i32 s23, s23, 8
	s_lshl_b32 s24, s22, 11
	s_lshl_b32 s25, s23, 22
	s_add_u32 s24, s24, s25
	s_add_u32 s58, s64, s24
	s_addc_u32 s59, s65, 0
	s_lshl_b32 s24, s22, 10
	s_lshl_b32 s25, s23, 21
	s_add_u32 s24, s24, s25
	s_add_u32 s60, s66, s24
	s_addc_u32 s61, s67, 0
	global_load_dwordx4 v[64:67], v1, s[58:59] nt
	global_load_dwordx4 v[68:71], v1, s[58:59] offset:1024 nt
	s_add_i32 s21, s21, s27
	s_add_i32 s26, s26, 1
.Las_issued:
	s_waitcnt vmcnt(0)
	s_cmp_le_u32 s26, 0
	s_cbranch_scc1 .Las_stored
	v_cvt_pk_f16_f32 v8, v8, v9
	v_cvt_pk_f16_f32 v9, v10, v11
	v_cvt_pk_f16_f32 v10, v12, v13
	v_cvt_pk_f16_f32 v11, v14, v15
	global_store_dwordx2 v2, v[8:9], s[32:33]
	global_store_dwordx2 v2, v[10:11], s[32:33] offset:512
	s_cmp_le_u32 s26, 1
	s_cbranch_scc1 .Las_stored
	v_cvt_pk_f16_f32 v16, v16, v17
	v_cvt_pk_f16_f32 v17, v18, v19
	v_cvt_pk_f16_f32 v18, v20, v21
	v_cvt_pk_f16_f32 v19, v22, v23
	global_store_dwordx2 v2, v[16:17], s[36:37]
	global_store_dwordx2 v2, v[18:19], s[36:37] offset:512
	s_cmp_le_u32 s26, 2
	s_cbranch_scc1 .Las_stored
	v_cvt_pk_f16_f32 v24, v24, v25
	v_cvt_pk_f16_f32 v25, v26, v27
	v_cvt_pk_f16_f32 v26, v28, v29
	v_cvt_pk_f16_f32 v27, v30, v31
	global_store_dwordx2 v2, v[24:25], s[40:41]
	global_store_dwordx2 v2, v[26:27], s[40:41] offset:512
	s_cmp_le_u32 s26, 3
	s_cbranch_scc1 .Las_stored
	v_cvt_pk_f16_f32 v32, v32, v33
	v_cvt_pk_f16_f32 v33, v34, v35
	v_cvt_pk_f16_f32 v34, v36, v37
	v_cvt_pk_f16_f32 v35, v38, v39
	global_store_dwordx2 v2, v[32:33], s[44:45]
	global_store_dwordx2 v2, v[34:35], s[44:45] offset:512
	s_cmp_le_u32 s26, 4
	s_cbranch_scc1 .Las_stored
	v_cvt_pk_f16_f32 v40, v40, v41
	v_cvt_pk_f16_f32 v41, v42, v43
	v_cvt_pk_f16_f32 v42, v44, v45
	v_cvt_pk_f16_f32 v43, v46, v47
	global_store_dwordx2 v2, v[40:41], s[48:49]
	global_store_dwordx2 v2, v[42:43], s[48:49] offset:512
	s_cmp_le_u32 s26, 5
	s_cbranch_scc1 .Las_stored
	v_cvt_pk_f16_f32 v48, v48, v49
	v_cvt_pk_f16_f32 v49, v50, v51
	v_cvt_pk_f16_f32 v50, v52, v53
	v_cvt_pk_f16_f32 v51, v54, v55
	global_store_dwordx2 v2, v[48:49], s[52:53]
	global_store_dwordx2 v2, v[50:51], s[52:53] offset:512
	s_cmp_le_u32 s26, 6
	s_cbranch_scc1 .Las_stored
	v_cvt_pk_f16_f32 v56, v56, v57
	v_cvt_pk_f16_f32 v57, v58, v59
	v_cvt_pk_f16_f32 v58, v60, v61
	v_cvt_pk_f16_f32 v59, v62, v63
	global_store_dwordx2 v2, v[56:57], s[56:57]
	global_store_dwordx2 v2, v[58:59], s[56:57] offset:512
	s_cmp_le_u32 s26, 7
	s_cbranch_scc1 .Las_stored
	v_cvt_pk_f16_f32 v64, v64, v65
	v_cvt_pk_f16_f32 v65, v66, v67
	v_cvt_pk_f16_f32 v66, v68, v69
	v_cvt_pk_f16_f32 v67, v70, v71
	global_store_dwordx2 v2, v[64:65], s[60:61]
	global_store_dwordx2 v2, v[66:67], s[60:61] offset:512
.Las_stored:
	s_lshl_b32 s24, s27, 3
	s_add_i32 s20, s20, s24
	s_branch .Las_trip
